# P0 dense-weight copy items rebalanced toward the 64 workgroups without adaLN GEMV work
# baseline (speedup 1.0000x reference)
; #define LAS __attribute__((address_space(3)))
; __device__ __forceinline__ void p0_convert(Frame& F, const Args& A) {
;     ...
;     { __syncthreads(); LAS float* scr8 = (LAS float*)(F.lds + F.wave * 16896); f32x4 va[16];
;       constexpr int NF8 = 16 * NLF * 32;
;       constexpr int NO8 = P6_F8 ? 16 * 64 : 0, NAB8 = P5_F8 ? 2 * 8 * 64 : 0;
; #pragma unroll 1
;       for (int it = gw; it < NF8 + NO8 + NAB8; it += NGW) {
;           if (it >= NF8 + NO8) { const int j = it - NF8 - NO8, br = j >> 9, jj = j & 511, k0 = (jj >> 6) * 128, n0 = (jj & 63) * 32;
;               cvt8_load(va, br ? A.in[I_WOB] : A.in[I_WOA], k0, n0, F.lane, DM); cvt8_store(va, br ? WSP(unsigned char, WS_WBT) : WSP(unsigned char, WS_WAT), k0, n0, scr8, F.lane, 1024); continue; }
;           if (it < NF8) { const int k0 = (it / (NLF * 32)) * 128, blk = it % (NLF * 32), pf = blk >> 5, g_ = (int)((LFMAP >> (4 * pf)) & 15ull);
;               cvt8_load(va, A.in[I_WIN], k0, g_ * 1024 + (blk & 31) * 32, F.lane, NQKV); cvt8_store(va, WSP(unsigned char, WS_WING), k0, pf * 1024 + (blk & 31) * 32, scr8, F.lane); }
;           else { const int j = it - NF8, k0 = (j >> 6) * 128, n0 = (j & 63) * 32;
;               cvt8_load(va, A.in[I_WO], k0, n0, F.lane, DM); cvt8_store(va, WSP(unsigned char, WS_WOT), k0, n0, scr8, F.lane); } } }
.LBB0_25:
	s_or_b64 exec, exec, s[4:5]
	s_lshl_b32 s0, s90, 3
	v_readlane_b32 s1, v246, 40
	s_add_i32 s0, s0, s1
	s_cmpk_lt_i32 s0, 0x1c00
	s_barrier
	s_cbranch_scc0 .LBB0_36
	v_readlane_b32 s2, v246, 40
	s_mulk_i32 s2, 0x4200
	s_add_i32 s2, s2, 0
	v_and_b32_e32 v5, 7, v0
	v_lshrrev_b32_e32 v14, 3, v1
	v_lshlrev_b32_e32 v10, 2, v5
	s_movk_i32 s3, 0x84
	v_mov_b32_e32 v6, s2
	v_mad_u32_u24 v7, v14, s3, v6
	v_add_u32_e32 v9, 4, v10
	v_add_u32_e32 v8, 0x840, v7
	v_and_b32_e32 v9, 28, v9
	v_lshl_add_u32 v19, v9, 2, v8
	v_add_u32_e32 v9, 6, v10
	v_and_b32_e32 v9, 28, v9
	s_movk_i32 s2, 0x420
	v_lshlrev_b32_e32 v9, 2, v9
	v_add3_u32 v21, v8, v9, s2
	v_add_u32_e32 v8, 8, v10
	v_and_b32_e32 v8, 28, v8
	v_lshl_add_u32 v11, v8, 2, v7
	v_add_u32_e32 v8, 10, v10
	v_and_b32_e32 v8, 28, v8
	v_lshl_add_u32 v12, v8, 2, v7
	v_add_u32_e32 v8, 12, v10
	v_and_b32_e32 v8, 28, v8
	v_lshl_add_u32 v13, v8, 2, v7
	v_add_u32_e32 v8, 14, v10
	v_and_b32_e32 v8, 28, v8
	v_lshl_add_u32 v37, v8, 2, v7
	v_add_u32_e32 v8, 18, v10
	v_and_b32_e32 v8, 28, v8
	v_lshl_add_u32 v41, v8, 2, v7
	v_add_u32_e32 v8, 20, v10
	v_and_b32_e32 v8, 28, v8
	v_lshl_add_u32 v43, v8, 2, v7
	v_add_u32_e32 v8, 22, v10
	v_and_b32_e32 v8, 28, v8
	v_lshl_add_u32 v45, v8, 2, v7
	v_add_u32_e32 v8, 24, v10
	v_and_b32_e32 v8, 28, v8
	v_lshl_add_u32 v22, v8, 2, v7
	v_add_u32_e32 v8, 26, v10
	v_and_b32_e32 v8, 28, v8
	v_lshl_add_u32 v23, v8, 2, v7
	v_add_u32_e32 v8, 28, v10
	v_and_b32_e32 v8, 28, v8
	v_mov_b32_e32 v3, 0
	s_movk_i32 s3, 0x840
	v_lshl_add_u32 v24, v8, 2, v7
	v_add_u32_e32 v8, 30, v10
	v_lshlrev_b32_e32 v4, 4, v5
	v_or_b32_e32 v16, 8, v14
	v_or_b32_e32 v18, 16, v14
	v_or_b32_e32 v20, 24, v14
	v_and_b32_e32 v8, 28, v8
	v_mad_u32_u24 v29, v5, s3, v6
	v_mov_b32_e32 v5, v3
	v_lshl_add_u32 v25, v8, 2, v7
	v_lshl_add_u64 v[8:9], s[30:31], 0, v[4:5]
	s_mov_b64 s[2:3], 0x3400000
	v_add_u32_e32 v26, v10, v14
	v_add_u32_e32 v27, v16, v10
	v_add_u32_e32 v28, v18, v10
	v_add_u32_e32 v10, v20, v10
	v_and_b32_e32 v2, 28, v194
	v_add_u32_e32 v15, v7, v4
	v_xad_u32 v39, v4, 64, v7
	v_lshl_add_u64 v[6:7], v[8:9], 0, s[2:3]
	v_and_b32_e32 v26, 31, v26
	v_and_b32_e32 v27, 31, v27
	v_and_b32_e32 v28, 31, v28
	v_and_b32_e32 v10, 31, v10
	s_mov_b64 s[2:3], 0x400000
	s_mov_b32 s6, 0x76543210
	s_movk_i32 s1, 0x200
	s_cmpk_ge_i32 s90, 0xc0
	s_cselect_b32 s1, s1, 0x100000
	s_mov_b32 s5, 0
	v_add_u32_e32 v17, 0x420, v15
	v_lshl_add_u32 v26, v26, 2, v29
	v_lshl_add_u32 v27, v27, 2, v29
	v_lshl_add_u32 v28, v28, 2, v29
	v_lshl_add_u32 v29, v10, 2, v29
	v_lshl_add_u64 v[8:9], v[8:9], 0, s[2:3]
	s_lshl_b32 s2, s0, 5
	s_lshl_b32 s3, s1, 5
	s_lshl_b32 s10, s0, 1
	s_lshl_b32 s11, s1, 1
	s_mov_b32 s33, 0x40000
	s_mov_b32 s34, 0x50000
	s_mov_b32 s35, 0x60000
	s_mov_b32 s36, 0x70000
	s_mov_b32 s37, 0x80000
	s_mov_b32 s38, 0x90000
	s_mov_b32 s39, 0xa0000
	s_mov_b32 s40, 0xb0000
	s_mov_b32 s41, 0xc0000
	s_mov_b32 s42, 0xd0000
	s_mov_b32 s43, 0xe0000
	s_mov_b32 s44, 0xf0000
	v_add_u32_e32 v30, 0x1080, v11
	v_add_u32_e32 v31, 0x1088, v11
	v_add_u32_e32 v32, 0x14a0, v12
	v_add_u32_e32 v33, 0x14a8, v12
	v_add_u32_e32 v34, 0x18c0, v13
	v_add_u32_e32 v35, 0x18c8, v13
	v_add_u32_e32 v36, 0x1ce0, v37
	v_add_u32_e32 v37, 0x1ce8, v37
	v_add_u32_e32 v38, 0x2100, v39
	v_add_u32_e32 v39, 0x2108, v39
	v_add_u32_e32 v40, 0x2520, v41
	v_add_u32_e32 v41, 0x2528, v41
	v_add_u32_e32 v42, 0x2940, v43
	v_add_u32_e32 v43, 0x2948, v43
	v_add_u32_e32 v44, 0x2d60, v45
	v_add_u32_e32 v45, 0x2d68, v45
	s_movk_i32 s7, 0x98
	s_mov_b32 s45, 0xa000
	s_mov_b32 s46, 0x140000
	s_mov_b32 s47, 0x190000
	s_mov_b32 s48, 0x1e0000
	s_mov_b32 s49, 0x230000
	s_mov_b32 s50, 0x280000
	s_mov_b32 s51, 0x2d0000
	s_mov_b32 s52, 0x320000
	s_mov_b32 s53, 0x370000
	s_mov_b32 s54, 0x3c0000
	s_mov_b32 s55, 0x410000
	s_mov_b32 s56, 0x460000
	s_mov_b32 s57, 0x4b0000
	s_mov_b32 s58, 0x2c00000
	v_lshlrev_b32_e32 v10, 2, v2
	v_add_u32_e32 v46, 0x3180, v22
	s_branch .LBB0_28
